# three small latency edits: S3 first-block barrier skipped, router bias load hoisted before the logits loop, first late hb load in rwkv_out issued with the initial batch
# baseline (speedup 1.0000x reference)
.LBB0_635:
	s_or_b64 exec, exec, s[12:13]
	s_waitcnt lgkmcnt(0)
	s_cmp_eq_u32 s11, 0
	s_cbranch_scc1 .Ls3_nobar
	s_barrier
.Ls3_nobar:
	s_and_saveexec_b64 s[12:13], s[0:1]
	s_cbranch_execz .LBB0_624
	s_andn2_b64 vcc, exec, s[4:5]
	s_cbranch_vccnz .LBB0_623
	ds_read2st64_b32 v[18:19], v168 offset1:2
	ds_read2st64_b32 v[20:21], v168 offset0:4 offset1:6
	ds_read2st64_b32 v[22:23], v168 offset0:8 offset1:10
	ds_read2st64_b32 v[24:25], v168 offset0:28 offset1:30
	ds_read2st64_b32 v[26:27], v168 offset0:24 offset1:26
	ds_read2st64_b32 v[28:29], v168 offset0:20 offset1:22
	ds_read2st64_b32 v[30:31], v168 offset0:16 offset1:18
	ds_read2st64_b32 v[32:33], v168 offset0:12 offset1:14
	s_waitcnt lgkmcnt(4)
	v_pk_add_f32 v[16:17], v[16:17], v[24:25]
	s_waitcnt lgkmcnt(3)
	v_pk_add_f32 v[14:15], v[14:15], v[26:27]
	s_waitcnt lgkmcnt(2)
	v_pk_add_f32 v[12:13], v[12:13], v[28:29]
	s_waitcnt lgkmcnt(1)
	v_pk_add_f32 v[10:11], v[10:11], v[30:31]
	s_waitcnt lgkmcnt(0)
	v_pk_add_f32 v[8:9], v[8:9], v[32:33]
	v_pk_add_f32 v[6:7], v[6:7], v[22:23]
	v_pk_add_f32 v[4:5], v[4:5], v[20:21]
	v_pk_add_f32 v[2:3], v[2:3], v[18:19]
	s_branch .LBB0_623

.LBB0_1203:
	v_ashrrev_i32_e32 v2, 31, v196
	v_lshrrev_b32_e32 v2, 26, v2
	v_add_u32_e32 v2, v196, v2
	v_ashrrev_i32_e32 v3, 6, v2
	v_and_b32_e32 v2, 0xffffffc0, v2
	v_sub_u32_e32 v193, v196, v2
	v_mul_hi_i32 v2, v3, s26
	v_lshrrev_b32_e32 v4, 31, v2
	v_add_u32_e32 v2, v2, v4
	v_mul_lo_u32 v2, v2, 6
	v_sub_u32_e32 v192, v3, v2
	v_mul_hi_i32 v2, v196, s26
	v_lshrrev_b32_e32 v3, 31, v2
	v_ashrrev_i32_e32 v2, 6, v2
	v_add_u32_e32 v202, v2, v3
	v_mul_i32_i24_e32 v2, 6, v202
	v_add_lshl_u32 v100, v2, v192, 6
	v_add_u32_e32 v2, v100, v193
	v_ashrrev_i32_e32 v3, 31, v2
	v_lshlrev_b64 v[6:7], 13, v[2:3]
	v_lshl_add_u64 v[94:95], s[10:11], 0, v[6:7]
	v_mov_b32_e32 v171, v1
	v_lshl_add_u64 v[96:97], s[8:9], 0, v[6:7]
	v_mov_b32_e32 v157, v1
	v_lshl_add_u64 v[52:53], v[94:95], 0, v[170:171]
	v_lshl_add_u64 v[46:47], v[96:97], 0, v[156:157]
	global_load_dwordx2 v[12:13], v[52:53], off
	global_load_dwordx4 v[2:5], v[46:47], off
	v_lshl_add_u64 v[6:7], v[154:155], 0, v[6:7]
	v_mov_b32_e32 v163, v1
	v_mov_b32_e32 v167, v1
	v_mov_b32_e32 v159, v1
	v_lshl_add_u64 v[70:71], v[6:7], 0, v[0:1]
	v_lshl_add_u64 v[72:73], v[6:7], 0, v[162:163]
	v_lshl_add_u64 v[86:87], v[6:7], 0, v[166:167]
	v_lshl_add_u64 v[6:7], v[96:97], 0, v[158:159]
	global_load_dwordx2 v[16:17], v[52:53], off offset:512
	global_load_dwordx2 v[20:21], v[52:53], off offset:1024
	global_load_dwordx4 v[54:57], v[70:71], off
	global_load_dwordx2 v[24:25], v[52:53], off offset:1536
	global_load_dwordx4 v[58:61], v[70:71], off offset:2048
	global_load_dwordx4 v[30:33], v[46:47], off offset:1024
	global_load_dwordx4 v[62:65], v[72:73], off
	global_load_dwordx2 v[28:29], v[52:53], off offset:2048
	global_load_dwordx4 v[66:69], v[86:87], off
	global_load_dwordx2 v[42:43], v[52:53], off offset:2560
	global_load_dwordx2 v[48:49], v[52:53], off offset:3072
	global_load_dwordx2 v[246:247], v[52:53], off offset:3584
	global_load_dwordx4 v[82:85], v[70:71], off offset:16
	v_mov_b32_e32 v161, v1
	global_load_dwordx4 v[6:9], v[6:7], off
	v_mov_b32_e32 v173, v1
	global_load_dwordx4 v[78:81], v[70:71], off offset:2064
	global_load_dwordx4 v[74:77], v[72:73], off offset:16
	v_mov_b32_e32 v165, v1
	global_load_dwordx4 v[70:73], v[86:87], off offset:16
	v_mov_b32_e32 v175, v1
	v_mov_b32_e32 v177, v1
	v_mov_b32_e32 v179, v1
	v_lshl_add_u64 v[98:99], v[94:95], 0, v[178:179]
	v_mov_b32_e32 v181, v1
	v_mov_b32_e32 v169, v1
	v_mov_b32_e32 v189, v1
	v_mov_b32_e32 v187, v1
	v_mov_b32_e32 v191, v1
	s_mov_b32 s25, 0
	s_mov_b64 s[0:1], -1
	s_waitcnt vmcnt(17)
	v_lshlrev_b32_e32 v10, 16, v12
	v_and_b32_e32 v11, 0xffff0000, v12
	v_lshlrev_b32_e32 v12, 16, v13
	v_and_b32_e32 v13, 0xffff0000, v13
	s_waitcnt vmcnt(15)
	v_lshlrev_b32_e32 v14, 16, v16
	s_waitcnt vmcnt(13)
	v_mfma_f32_16x16x32_bf16 v[10:13], v[2:5], v[54:57], v[10:13]
	v_and_b32_e32 v15, 0xffff0000, v16
	s_waitcnt vmcnt(8)
	v_lshlrev_b32_e32 v26, 16, v28
	v_and_b32_e32 v27, 0xffff0000, v28
	v_lshlrev_b32_e32 v28, 16, v29
	v_and_b32_e32 v29, 0xffff0000, v29
	v_lshlrev_b32_e32 v16, 16, v17
	v_and_b32_e32 v17, 0xffff0000, v17
	v_mfma_f32_16x16x32_bf16 v[38:41], v[30:33], v[54:57], v[26:29]
	v_lshlrev_b32_e32 v18, 16, v20
	v_and_b32_e32 v19, 0xffff0000, v20
	v_lshlrev_b32_e32 v20, 16, v21
	s_waitcnt vmcnt(5)
	v_lshlrev_b32_e32 v26, 16, v48
	v_and_b32_e32 v27, 0xffff0000, v48
	v_lshlrev_b32_e32 v28, 16, v49
	v_and_b32_e32 v29, 0xffff0000, v49
	v_and_b32_e32 v21, 0xffff0000, v21
	v_lshlrev_b32_e32 v22, 16, v24
	v_mfma_f32_16x16x32_bf16 v[48:51], v[30:33], v[62:65], v[26:29]
	v_and_b32_e32 v23, 0xffff0000, v24
	v_lshlrev_b32_e32 v24, 16, v25
	v_and_b32_e32 v25, 0xffff0000, v25
	s_waitcnt vmcnt(3)
	v_mfma_f32_16x16x32_bf16 v[26:29], v[6:9], v[82:85], v[10:13]
	s_nop 2
	v_lshl_add_u64 v[10:11], v[96:97], 0, v[160:161]
	global_load_dwordx4 v[86:89], v[10:11], off
	v_mfma_f32_16x16x32_bf16 v[14:17], v[2:5], v[58:61], v[14:17]
	v_mfma_f32_16x16x32_bf16 v[18:21], v[2:5], v[62:65], v[18:21]
	v_mfma_f32_16x16x32_bf16 v[2:5], v[2:5], v[66:69], v[22:25]
	s_nop 2
	v_lshlrev_b32_e32 v22, 16, v42
	v_and_b32_e32 v23, 0xffff0000, v42
	v_lshlrev_b32_e32 v24, 16, v43
	v_and_b32_e32 v25, 0xffff0000, v43
	s_waitcnt vmcnt(2)
	v_mfma_f32_16x16x32_bf16 v[18:21], v[6:9], v[74:77], v[18:21]
	v_mfma_f32_16x16x32_bf16 v[42:45], v[30:33], v[58:61], v[22:25]
	v_mfma_f32_16x16x32_bf16 v[22:25], v[6:9], v[78:81], v[14:17]
	s_waitcnt vmcnt(1)
	v_mfma_f32_16x16x32_bf16 v[14:17], v[6:9], v[70:73], v[2:5]
	s_nop 2
	v_lshl_add_u64 v[2:3], v[94:95], 0, v[172:173]
	s_waitcnt vmcnt(0)
	v_mfma_f32_16x16x32_bf16 v[10:13], v[86:89], v[82:85], v[38:41]
	s_nop 2
	s_nop 0
	s_waitcnt vmcnt(0)
	v_lshlrev_b32_e32 v38, 16, v246
	v_and_b32_e32 v39, 0xffff0000, v246
	v_lshlrev_b32_e32 v40, 16, v247
	v_and_b32_e32 v41, 0xffff0000, v247
	v_mfma_f32_16x16x32_bf16 v[6:9], v[86:89], v[78:81], v[42:45]
	s_nop 0
	v_mfma_f32_16x16x32_bf16 v[30:33], v[30:33], v[66:69], v[38:41]
	s_nop 0
	global_load_dwordx2 v[42:43], v[2:3], off
	v_lshl_add_u64 v[44:45], v[94:95], 0, v[174:175]
	v_lshl_add_u64 v[40:41], v[96:97], 0, v[164:165]
	global_load_dwordx4 v[90:93], v[40:41], off
	v_mfma_f32_16x16x32_bf16 v[2:5], v[86:89], v[74:77], v[48:51]
	v_lshl_add_u64 v[96:97], v[96:97], 0, v[168:169]
	s_waitcnt vmcnt(1)
	v_lshlrev_b32_e32 v38, 16, v42
	global_load_dwordx4 v[50:53], v[46:47], off offset:2048
	global_load_dwordx2 v[48:49], v[44:45], off
	v_and_b32_e32 v39, 0xffff0000, v42
	v_lshlrev_b32_e32 v40, 16, v43
	v_and_b32_e32 v41, 0xffff0000, v43
	v_mfma_f32_16x16x32_bf16 v[30:33], v[86:89], v[70:73], v[30:33]
	v_lshl_add_u64 v[86:87], v[94:95], 0, v[176:177]
	s_waitcnt vmcnt(1)
	v_mfma_f32_16x16x32_bf16 v[38:41], v[50:53], v[54:57], v[38:41]
	v_mfma_f32_16x16x32_bf16 v[42:45], v[90:93], v[82:85], v[38:41]
	s_waitcnt vmcnt(0)
	s_nop 5
	v_lshlrev_b32_e32 v38, 16, v48
	v_and_b32_e32 v39, 0xffff0000, v48
	v_lshlrev_b32_e32 v40, 16, v49
	v_and_b32_e32 v41, 0xffff0000, v49
	global_load_dwordx2 v[48:49], v[86:87], off
	s_waitcnt vmcnt(0)
	v_lshlrev_b32_e32 v86, 16, v48
	v_and_b32_e32 v87, 0xffff0000, v48
	v_lshlrev_b32_e32 v88, 16, v49
	v_and_b32_e32 v89, 0xffff0000, v49
	v_mfma_f32_16x16x32_bf16 v[38:41], v[50:53], v[58:61], v[38:41]
	s_nop 0
	v_mfma_f32_16x16x32_bf16 v[102:105], v[50:53], v[62:65], v[86:89]
	global_load_dwordx2 v[108:109], v[98:99], off
	s_nop 1
	global_load_dwordx4 v[86:89], v[46:47], off offset:3072
	v_lshl_add_u64 v[98:99], v[94:95], 0, v[180:181]
	global_load_dwordx2 v[98:99], v[98:99], off
	v_mfma_f32_16x16x32_bf16 v[46:49], v[90:93], v[74:77], v[102:105]
	s_waitcnt vmcnt(2)
	v_lshlrev_b32_e32 v106, 16, v108
	v_and_b32_e32 v107, 0xffff0000, v108
	v_lshlrev_b32_e32 v108, 16, v109
	v_and_b32_e32 v109, 0xffff0000, v109
	global_load_dwordx4 v[102:105], v[96:97], off
	v_mfma_f32_16x16x32_bf16 v[38:41], v[90:93], v[78:81], v[38:41]
	v_mfma_f32_16x16x32_bf16 v[50:53], v[50:53], v[66:69], v[106:109]
	v_mfma_f32_16x16x32_bf16 v[50:53], v[90:93], v[70:73], v[50:53]
	v_lshl_add_u64 v[90:91], v[94:95], 0, v[188:189]
	s_nop 0
	global_load_dwordx2 v[106:107], v[90:91], off
	v_lshl_add_u64 v[96:97], v[94:95], 0, v[186:187]
	global_load_dwordx2 v[96:97], v[96:97], off
	s_waitcnt vmcnt(3)
	v_lshlrev_b32_e32 v90, 16, v98
	v_and_b32_e32 v91, 0xffff0000, v98
	v_lshlrev_b32_e32 v92, 16, v99
	v_and_b32_e32 v93, 0xffff0000, v99
	s_nop 1
	v_mfma_f32_16x16x32_bf16 v[54:57], v[86:89], v[54:57], v[90:93]
	s_nop 2
	v_lshl_add_u64 v[90:91], v[94:95], 0, v[190:191]
	global_load_dwordx2 v[98:99], v[90:91], off
	v_sub_u32_e32 v90, v100, v193
	v_add_u32_e32 v90, 0x63f, v90
	v_ashrrev_i32_e32 v91, 31, v90
	v_lshlrev_b64 v[90:91], 13, v[90:91]
	v_lshl_add_u64 v[146:147], s[8:9], 0, v[90:91]
	v_lshl_add_u64 v[194:195], s[10:11], 0, v[90:91]
	v_lshl_add_u64 v[148:149], v[146:147], 0, v[156:157]
	v_lshl_add_u64 v[118:119], v[194:195], 0, v[170:171]
	global_load_dwordx4 v[114:117], v[148:149], off
	global_load_dwordx2 v[108:109], v[118:119], off
	s_waitcnt vmcnt(5)
	v_mfma_f32_16x16x32_bf16 v[54:57], v[102:105], v[82:85], v[54:57]
	v_lshl_add_u64 v[110:111], v[154:155], 0, v[90:91]
	v_lshl_add_u64 v[100:101], v[110:111], 0, v[0:1]
	global_load_dwordx4 v[126:129], v[100:101], off
	v_lshl_add_u64 v[144:145], v[194:195], 0, v[176:177]
	v_lshl_add_u64 v[184:185], v[194:195], 0, v[178:179]
	v_lshl_add_u64 v[210:211], v[194:195], 0, v[186:187]
	s_waitcnt vmcnt(4)
	v_lshlrev_b32_e32 v82, 16, v96
	v_and_b32_e32 v83, 0xffff0000, v96
	v_lshlrev_b32_e32 v84, 16, v97
	v_and_b32_e32 v85, 0xffff0000, v97
	s_nop 1
	v_mfma_f32_16x16x32_bf16 v[58:61], v[86:89], v[58:61], v[82:85]
	v_mfma_f32_16x16x32_bf16 v[58:61], v[102:105], v[78:81], v[58:61]
	v_lshlrev_b32_e32 v78, 16, v106
	v_and_b32_e32 v79, 0xffff0000, v106
	v_lshlrev_b32_e32 v80, 16, v107
	v_and_b32_e32 v81, 0xffff0000, v107
	v_lshl_add_u64 v[82:83], v[146:147], 0, v[158:159]
	global_load_dwordx4 v[82:85], v[82:83], off
	v_mfma_f32_16x16x32_bf16 v[62:65], v[86:89], v[62:65], v[78:81]
	global_load_dwordx4 v[94:97], v[100:101], off offset:16
	s_nop 1
	global_load_dwordx2 v[78:79], v[118:119], off offset:512
	global_load_dwordx4 v[90:93], v[100:101], off offset:2048
	v_mfma_f32_16x16x32_bf16 v[62:65], v[102:105], v[74:77], v[62:65]
	s_waitcnt vmcnt(7)
	v_lshlrev_b32_e32 v74, 16, v98
	v_and_b32_e32 v75, 0xffff0000, v98
	v_lshlrev_b32_e32 v76, 16, v99
	v_and_b32_e32 v77, 0xffff0000, v99
	global_load_dwordx4 v[98:101], v[100:101], off offset:2064
	s_nop 0
	global_load_dwordx2 v[80:81], v[118:119], off offset:1024
	v_mfma_f32_16x16x32_bf16 v[66:69], v[86:89], v[66:69], v[74:77]
	v_lshl_add_u64 v[86:87], v[110:111], 0, v[162:163]
	v_lshl_add_u64 v[110:111], v[110:111], 0, v[166:167]
	v_mfma_f32_16x16x32_bf16 v[66:69], v[102:105], v[70:73], v[66:69]
	s_waitcnt vmcnt(7)
	v_lshlrev_b32_e32 v70, 16, v108
	v_and_b32_e32 v71, 0xffff0000, v108
	v_lshlrev_b32_e32 v72, 16, v109
	v_and_b32_e32 v73, 0xffff0000, v109
	global_load_dwordx4 v[106:109], v[86:87], off
	s_nop 0
	global_load_dwordx4 v[86:89], v[86:87], off offset:16
	s_nop 0
	global_load_dwordx2 v[122:123], v[118:119], off offset:1536
	global_load_dwordx4 v[102:105], v[110:111], off
	global_load_dwordx4 v[130:133], v[148:149], off offset:1024
	s_nop 0
	global_load_dwordx4 v[110:113], v[110:111], off offset:16
	s_waitcnt vmcnt(12)
	v_mfma_f32_16x16x32_bf16 v[70:73], v[114:117], v[126:129], v[70:73]
	global_load_dwordx2 v[140:141], v[118:119], off offset:3072
	global_load_dwordx2 v[142:143], v[118:119], off offset:3584
	s_waitcnt vmcnt(11)
	v_lshlrev_b32_e32 v74, 16, v78
	v_and_b32_e32 v75, 0xffff0000, v78
	v_lshlrev_b32_e32 v76, 16, v79
	v_and_b32_e32 v77, 0xffff0000, v79
	v_mfma_f32_16x16x32_bf16 v[70:73], v[82:85], v[94:97], v[70:73]
	s_waitcnt vmcnt(8)
	v_lshlrev_b32_e32 v78, 16, v80
	v_and_b32_e32 v79, 0xffff0000, v80
	v_lshlrev_b32_e32 v80, 16, v81
	v_and_b32_e32 v81, 0xffff0000, v81
	v_mfma_f32_16x16x32_bf16 v[74:77], v[114:117], v[90:93], v[74:77]
	s_nop 1
	ds_bpermute_b32 v73, v198, v73
	ds_bpermute_b32 v72, v198, v72
	ds_bpermute_b32 v71, v198, v71
	s_waitcnt vmcnt(7)
	v_mfma_f32_16x16x32_bf16 v[78:81], v[114:117], v[106:109], v[78:81]
	s_waitcnt vmcnt(5)
	v_lshlrev_b32_e32 v120, 16, v122
	v_and_b32_e32 v121, 0xffff0000, v122
	v_lshlrev_b32_e32 v122, 16, v123
	v_and_b32_e32 v123, 0xffff0000, v123
	v_mfma_f32_16x16x32_bf16 v[74:77], v[82:85], v[98:101], v[74:77]
	s_waitcnt lgkmcnt(2)
	v_add_f32_e32 v54, v54, v73
	ds_bpermute_b32 v70, v198, v70
	s_waitcnt lgkmcnt(2)
	v_add_f32_e32 v55, v55, v72
	s_waitcnt vmcnt(4)
	v_mfma_f32_16x16x32_bf16 v[114:117], v[114:117], v[102:105], v[120:123]
	s_waitcnt lgkmcnt(1)
	v_add_f32_e32 v56, v56, v71
	ds_bpermute_b32 v73, v198, v77
	s_waitcnt lgkmcnt(1)
	v_add_f32_e32 v57, v57, v70
	v_lshl_add_u64 v[122:123], v[146:147], 0, v[160:161]
	global_load_dwordx2 v[120:121], v[118:119], off offset:2048
	global_load_dwordx4 v[134:137], v[122:123], off
	v_mfma_f32_16x16x32_bf16 v[78:81], v[82:85], v[86:89], v[78:81]
	global_load_dwordx2 v[122:123], v[118:119], off offset:2560
	s_waitcnt lgkmcnt(0)
	v_add_f32_e32 v58, v58, v73
	ds_bpermute_b32 v70, v198, v75
	s_waitcnt vmcnt(5)
	v_mfma_f32_16x16x32_bf16 v[82:85], v[82:85], v[110:113], v[114:117]
	ds_bpermute_b32 v71, v198, v74
	s_nop 0
	ds_bpermute_b32 v72, v198, v81
	ds_bpermute_b32 v73, v198, v80
	ds_bpermute_b32 v74, v198, v79
	ds_bpermute_b32 v76, v198, v76
	s_waitcnt lgkmcnt(5)
	v_add_f32_e32 v60, v60, v70
	s_waitcnt lgkmcnt(4)
	v_add_f32_e32 v61, v61, v71
	s_waitcnt lgkmcnt(3)
	v_add_f32_e32 v62, v62, v72
	s_waitcnt lgkmcnt(2)
	v_add_f32_e32 v63, v63, v73
	s_waitcnt lgkmcnt(1)
	v_add_f32_e32 v64, v64, v74
	ds_bpermute_b32 v70, v198, v78
	ds_bpermute_b32 v71, v198, v85
	ds_bpermute_b32 v72, v198, v84
	ds_bpermute_b32 v73, v198, v83
	ds_bpermute_b32 v74, v198, v82
	s_waitcnt lgkmcnt(5)
	v_add_f32_e32 v59, v59, v76
	s_waitcnt lgkmcnt(4)
	v_add_f32_e32 v65, v65, v70
	s_waitcnt lgkmcnt(3)
	v_add_f32_e32 v66, v66, v71
	s_waitcnt vmcnt(4)
	v_lshlrev_b32_e32 v138, 16, v140
	v_and_b32_e32 v139, 0xffff0000, v140
	v_lshlrev_b32_e32 v140, 16, v141
	v_and_b32_e32 v141, 0xffff0000, v141
	s_waitcnt lgkmcnt(2)
	v_add_f32_e32 v67, v67, v72
	s_waitcnt lgkmcnt(1)
	v_add_f32_e32 v68, v68, v73
	v_mfma_f32_16x16x32_bf16 v[138:141], v[130:133], v[106:109], v[138:141]
	s_waitcnt lgkmcnt(0)
	v_add_f32_e32 v69, v69, v74
	s_waitcnt vmcnt(2)
	v_lshlrev_b32_e32 v114, 16, v120
	v_and_b32_e32 v115, 0xffff0000, v120
	v_lshlrev_b32_e32 v116, 16, v121
	v_and_b32_e32 v117, 0xffff0000, v121
	s_waitcnt vmcnt(0)
	v_lshlrev_b32_e32 v120, 16, v122
	v_and_b32_e32 v121, 0xffff0000, v122
	v_lshlrev_b32_e32 v122, 16, v123
	v_and_b32_e32 v123, 0xffff0000, v123
	v_mfma_f32_16x16x32_bf16 v[114:117], v[130:133], v[126:129], v[114:117]
	s_nop 0
	v_mfma_f32_16x16x32_bf16 v[120:123], v[130:133], v[90:93], v[120:123]
	v_mfma_f32_16x16x32_bf16 v[122:125], v[134:137], v[98:101], v[120:123]
	v_mfma_f32_16x16x32_bf16 v[118:121], v[134:137], v[86:89], v[138:141]
	s_nop 2
	v_lshlrev_b32_e32 v138, 16, v142
	v_and_b32_e32 v139, 0xffff0000, v142
	v_lshlrev_b32_e32 v140, 16, v143
	v_and_b32_e32 v141, 0xffff0000, v143
	v_lshl_add_u64 v[142:143], v[194:195], 0, v[174:175]
	v_mfma_f32_16x16x32_bf16 v[114:117], v[134:137], v[94:97], v[114:117]
	v_mfma_f32_16x16x32_bf16 v[130:133], v[130:133], v[102:105], v[138:141]
	s_nop 2
	v_lshl_add_u64 v[138:139], v[194:195], 0, v[172:173]
	v_lshl_add_u64 v[140:141], v[146:147], 0, v[164:165]
	global_load_dwordx2 v[138:139], v[138:139], off
	s_nop 0
	global_load_dwordx4 v[150:153], v[148:149], off offset:2048
	global_load_dwordx4 v[224:227], v[140:141], off
	global_load_dwordx2 v[182:183], v[144:145], off
	v_mfma_f32_16x16x32_bf16 v[130:133], v[134:137], v[110:113], v[130:133]
	global_load_dwordx2 v[142:143], v[142:143], off
	s_waitcnt vmcnt(4)
	v_lshlrev_b32_e32 v134, 16, v138
	v_and_b32_e32 v135, 0xffff0000, v138
	v_lshlrev_b32_e32 v136, 16, v139
	v_and_b32_e32 v137, 0xffff0000, v139
	s_waitcnt vmcnt(3)
	s_nop 0
	v_mfma_f32_16x16x32_bf16 v[134:137], v[150:153], v[126:129], v[134:137]
	s_waitcnt vmcnt(2)
	v_mfma_f32_16x16x32_bf16 v[138:141], v[224:227], v[94:97], v[134:137]
	s_waitcnt vmcnt(0)
	s_nop 4
	v_lshlrev_b32_e32 v134, 16, v142
	v_and_b32_e32 v135, 0xffff0000, v142
	v_lshlrev_b32_e32 v136, 16, v143
	v_and_b32_e32 v137, 0xffff0000, v143
	s_nop 1
	v_mfma_f32_16x16x32_bf16 v[134:137], v[150:153], v[90:93], v[134:137]
	v_mfma_f32_16x16x32_bf16 v[142:145], v[224:227], v[98:101], v[134:137]
	s_nop 6
	v_lshlrev_b32_e32 v134, 16, v182
	v_and_b32_e32 v135, 0xffff0000, v182
	v_lshlrev_b32_e32 v136, 16, v183
	v_and_b32_e32 v137, 0xffff0000, v183
	global_load_dwordx2 v[182:183], v[184:185], off
	v_lshl_add_u64 v[184:185], v[146:147], 0, v[168:169]
	v_mfma_f32_16x16x32_bf16 v[134:137], v[150:153], v[106:109], v[134:137]
	s_waitcnt vmcnt(0)
	v_lshlrev_b32_e32 v228, 16, v182
	v_and_b32_e32 v229, 0xffff0000, v182
	v_lshlrev_b32_e32 v230, 16, v183
	v_and_b32_e32 v231, 0xffff0000, v183
	v_mfma_f32_16x16x32_bf16 v[134:137], v[224:227], v[86:89], v[134:137]
	s_nop 0
	v_mfma_f32_16x16x32_bf16 v[228:231], v[150:153], v[102:105], v[228:231]
	v_lshl_add_u64 v[150:151], v[194:195], 0, v[180:181]
	global_load_dwordx2 v[182:183], v[150:151], off
	s_nop 0
	global_load_dwordx4 v[150:153], v[148:149], off offset:3072
	v_mfma_f32_16x16x32_bf16 v[146:149], v[224:227], v[110:113], v[228:231]
	s_waitcnt vmcnt(1)
	v_lshlrev_b32_e32 v224, 16, v182
	s_nop 0
	global_load_dwordx4 v[228:231], v[184:185], off
	v_and_b32_e32 v225, 0xffff0000, v182
	v_lshlrev_b32_e32 v226, 16, v183
	v_and_b32_e32 v227, 0xffff0000, v183
	global_load_dwordx2 v[182:183], v[210:211], off
	v_lshl_add_u64 v[184:185], v[194:195], 0, v[188:189]
	s_waitcnt vmcnt(2)
	v_mfma_f32_16x16x32_bf16 v[126:129], v[150:153], v[126:129], v[224:227]
	s_waitcnt vmcnt(1)
	v_mfma_f32_16x16x32_bf16 v[94:97], v[228:231], v[94:97], v[126:129]
	s_waitcnt vmcnt(0)
	s_nop 4
	v_lshlrev_b32_e32 v126, 16, v182
	v_and_b32_e32 v127, 0xffff0000, v182
	v_lshlrev_b32_e32 v128, 16, v183
	v_and_b32_e32 v129, 0xffff0000, v183
	s_nop 1
	v_mfma_f32_16x16x32_bf16 v[90:93], v[150:153], v[90:93], v[126:129]
	s_nop 2
	global_load_dwordx2 v[126:127], v[184:185], off
	v_lshl_add_u64 v[128:129], v[194:195], 0, v[190:191]
	v_mfma_f32_16x16x32_bf16 v[90:93], v[228:231], v[98:101], v[90:93]
	s_waitcnt vmcnt(0)
	v_lshlrev_b32_e32 v98, 16, v126
	v_and_b32_e32 v99, 0xffff0000, v126
	v_lshlrev_b32_e32 v100, 16, v127
	v_and_b32_e32 v101, 0xffff0000, v127
	s_nop 2
	ds_bpermute_b32 v90, v198, v90
	ds_bpermute_b32 v93, v198, v93
	v_mfma_f32_16x16x32_bf16 v[98:101], v[150:153], v[106:109], v[98:101]
	global_load_dwordx2 v[106:107], v[128:129], off
	ds_bpermute_b32 v92, v198, v92
	s_waitcnt lgkmcnt(2)
	v_add_f32_e32 v25, v25, v90
	v_mfma_f32_16x16x32_bf16 v[86:89], v[228:231], v[86:89], v[98:101]
	ds_bpermute_b32 v91, v198, v91
	s_waitcnt lgkmcnt(2)
	v_add_f32_e32 v22, v22, v93
	s_waitcnt lgkmcnt(1)
	v_add_f32_e32 v23, v23, v92
	s_waitcnt lgkmcnt(0)
	v_add_f32_e32 v24, v24, v91
	s_waitcnt vmcnt(0)
	v_lshlrev_b32_e32 v98, 16, v106
	v_and_b32_e32 v99, 0xffff0000, v106
	v_lshlrev_b32_e32 v100, 16, v107
	v_and_b32_e32 v101, 0xffff0000, v107
	ds_bpermute_b32 v89, v198, v89
	ds_bpermute_b32 v88, v198, v88
	v_mfma_f32_16x16x32_bf16 v[98:101], v[150:153], v[102:105], v[98:101]
	ds_bpermute_b32 v102, v198, v97
	ds_bpermute_b32 v103, v198, v96
	ds_bpermute_b32 v104, v198, v95
	ds_bpermute_b32 v105, v198, v94
	v_mfma_f32_16x16x32_bf16 v[94:97], v[228:231], v[110:113], v[98:101]
	s_waitcnt lgkmcnt(5)
	v_add_f32_e32 v18, v18, v89
	ds_bpermute_b32 v87, v198, v87
	ds_bpermute_b32 v86, v198, v86
	s_waitcnt lgkmcnt(6)
	v_add_f32_e32 v19, v19, v88
	ds_bpermute_b32 v88, v198, v141
	s_nop 0
	ds_bpermute_b32 v89, v198, v97
	ds_bpermute_b32 v90, v198, v96
	s_waitcnt lgkmcnt(4)
	v_add_f32_e32 v20, v20, v87
	s_waitcnt lgkmcnt(3)
	v_add_f32_e32 v21, v21, v86
	ds_bpermute_b32 v86, v198, v95
	s_waitcnt lgkmcnt(2)
	v_add_f32_e32 v14, v14, v89
	ds_bpermute_b32 v87, v198, v94
	ds_bpermute_b32 v89, v198, v140
	s_waitcnt lgkmcnt(3)
	v_add_f32_e32 v15, v15, v90
	ds_bpermute_b32 v90, v198, v139
	s_waitcnt lgkmcnt(3)
	v_add_f32_e32 v16, v16, v86
	s_waitcnt lgkmcnt(2)
	v_add_f32_e32 v17, v17, v87
	v_add_f32_e32 v10, v10, v88
	s_waitcnt lgkmcnt(1)
	v_add_f32_e32 v11, v11, v89
	ds_bpermute_b32 v86, v198, v138
	ds_bpermute_b32 v87, v198, v145
	ds_bpermute_b32 v88, v198, v144
	ds_bpermute_b32 v89, v198, v143
	s_waitcnt lgkmcnt(4)
	v_add_f32_e32 v12, v12, v90
	ds_bpermute_b32 v90, v198, v142
	s_waitcnt lgkmcnt(4)
	v_add_f32_e32 v13, v13, v86
	s_waitcnt lgkmcnt(3)
	v_add_f32_e32 v6, v6, v87
	s_waitcnt lgkmcnt(2)
	v_add_f32_e32 v7, v7, v88
	s_waitcnt lgkmcnt(1)
	v_add_f32_e32 v8, v8, v89
	ds_bpermute_b32 v86, v198, v137
	ds_bpermute_b32 v87, v198, v136
	ds_bpermute_b32 v88, v198, v135
	ds_bpermute_b32 v89, v198, v134
	s_waitcnt lgkmcnt(4)
	v_add_f32_e32 v9, v9, v90
	ds_bpermute_b32 v90, v198, v149
	s_waitcnt lgkmcnt(4)
	v_add_f32_e32 v2, v2, v86
	s_waitcnt lgkmcnt(3)
	v_add_f32_e32 v3, v3, v87
	s_waitcnt lgkmcnt(2)
	v_add_f32_e32 v4, v4, v88
	s_waitcnt lgkmcnt(1)
	v_add_f32_e32 v5, v5, v89
	ds_bpermute_b32 v86, v198, v148
	ds_bpermute_b32 v87, v198, v147
	ds_bpermute_b32 v88, v198, v146
	ds_bpermute_b32 v89, v198, v117
	s_waitcnt lgkmcnt(4)
	v_add_f32_e32 v30, v30, v90
	ds_bpermute_b32 v90, v198, v116
	s_waitcnt lgkmcnt(4)
	v_add_f32_e32 v31, v31, v86
	s_waitcnt lgkmcnt(3)
	v_add_f32_e32 v32, v32, v87
	s_waitcnt lgkmcnt(2)
	v_add_f32_e32 v33, v33, v88
	s_waitcnt lgkmcnt(1)
	v_add_f32_e32 v42, v42, v89
	ds_bpermute_b32 v86, v198, v115
	ds_bpermute_b32 v87, v198, v114
	ds_bpermute_b32 v88, v198, v125
	ds_bpermute_b32 v89, v198, v124
	s_waitcnt lgkmcnt(4)
	v_add_f32_e32 v43, v43, v90
	ds_bpermute_b32 v90, v198, v123
	s_waitcnt lgkmcnt(4)
	v_add_f32_e32 v44, v44, v86
	s_waitcnt lgkmcnt(3)
	v_add_f32_e32 v45, v45, v87
	s_waitcnt lgkmcnt(2)
	v_add_f32_e32 v38, v38, v88
	s_waitcnt lgkmcnt(1)
	v_add_f32_e32 v39, v39, v89
	ds_bpermute_b32 v86, v198, v122
	ds_bpermute_b32 v87, v198, v121
	ds_bpermute_b32 v88, v198, v120
	ds_bpermute_b32 v89, v198, v119
	s_waitcnt lgkmcnt(4)
	v_add_f32_e32 v40, v40, v90
	ds_bpermute_b32 v90, v198, v118
	s_waitcnt lgkmcnt(4)
	v_add_f32_e32 v41, v41, v86
	s_waitcnt lgkmcnt(3)
	v_add_f32_e32 v46, v46, v87
	s_waitcnt lgkmcnt(2)
	v_add_f32_e32 v47, v47, v88
	s_waitcnt lgkmcnt(1)
	v_add_f32_e32 v48, v48, v89
	ds_bpermute_b32 v86, v198, v133
	ds_bpermute_b32 v87, v198, v132
	ds_bpermute_b32 v88, v198, v131
	ds_bpermute_b32 v89, v198, v130
	v_add_f32_e32 v26, v26, v102
	v_add_f32_e32 v27, v27, v103
	v_add_f32_e32 v28, v28, v104
	v_add_f32_e32 v29, v29, v105
	ds_write2_b32 v201, v26, v22 offset1:16
	ds_write2_b32 v201, v27, v23 offset0:68 offset1:84
	ds_write2_b32 v201, v28, v24 offset0:136 offset1:152
	ds_write2_b32 v201, v29, v25 offset0:204 offset1:220
	ds_write2_b32 v201, v18, v14 offset0:32 offset1:48
	ds_write2_b32 v201, v19, v15 offset0:100 offset1:116
	ds_write2_b32 v201, v20, v16 offset0:168 offset1:184
	ds_write2_b32 v201, v21, v17 offset0:236 offset1:252
	v_add_u32_e32 v14, 0x1000, v201
	ds_write2_b32 v14, v10, v6 offset0:64 offset1:80
	ds_write2_b32 v14, v11, v7 offset0:132 offset1:148
	ds_write2_b32 v14, v12, v8 offset0:200 offset1:216
	v_add_u32_e32 v6, 0x1400, v201
	v_lshl_or_b32 v10, v192, 6, v199
	ds_write2_b32 v6, v13, v9 offset0:12 offset1:28
	ds_write2_b32 v14, v2, v30 offset0:96 offset1:112
	ds_write2_b32 v14, v3, v31 offset0:164 offset1:180
	ds_write2_b32 v14, v4, v32 offset0:232 offset1:248
	ds_write2_b32 v6, v5, v33 offset0:44 offset1:60
	v_add_u32_e32 v2, 0x2000, v201
	v_add_u32_e32 v3, 0x2400, v201
	v_ashrrev_i32_e32 v11, 31, v10
	s_waitcnt lgkmcnt(14)
	v_add_f32_e32 v49, v49, v90
	v_add_f32_e32 v50, v50, v86
	v_add_f32_e32 v51, v51, v87
	v_add_f32_e32 v52, v52, v88
	v_add_f32_e32 v53, v53, v89
	ds_write2_b32 v2, v42, v38 offset0:128 offset1:144
	ds_write2_b32 v2, v43, v39 offset0:196 offset1:212
	ds_write2_b32 v3, v44, v40 offset0:8 offset1:24
	ds_write2_b32 v3, v45, v41 offset0:76 offset1:92
	ds_write2_b32 v2, v46, v50 offset0:160 offset1:176
	ds_write2_b32 v2, v47, v51 offset0:228 offset1:244
	ds_write2_b32 v3, v48, v52 offset0:40 offset1:56
	ds_write2_b32 v3, v49, v53 offset0:108 offset1:124
	v_add_u32_e32 v2, 0x3000, v201
	v_add_u32_e32 v3, 0x3400, v201
	v_lshlrev_b64 v[6:7], 2, v[10:11]
	ds_write2_b32 v2, v54, v58 offset0:192 offset1:208
	ds_write2_b32 v3, v55, v59 offset0:4 offset1:20
	ds_write2_b32 v3, v56, v60 offset0:72 offset1:88
	ds_write2_b32 v3, v57, v61 offset0:140 offset1:156
	ds_write2_b32 v2, v62, v66 offset0:224 offset1:240
	ds_write2_b32 v3, v63, v67 offset0:36 offset1:52
	ds_write2_b32 v3, v64, v68 offset0:104 offset1:120
	ds_write2_b32 v3, v65, v69 offset0:172 offset1:188
	v_lshl_add_u64 v[2:3], s[18:19], 0, v[6:7]
	v_lshl_add_u64 v[6:7], s[20:21], 0, v[6:7]
	global_load_dwordx4 v[2:5], v[2:3], off
	v_lshlrev_b32_e32 v12, 6, v193
	global_load_dwordx4 v[6:9], v[6:7], off
	v_lshl_add_u32 v23, v202, 12, v12
	v_lshlrev_b64 v[10:11], 1, v[10:11]
	v_ashrrev_i32_e32 v193, 31, v192
	v_or_b32_e32 v29, v23, v197
	v_lshl_add_u64 v[12:13], s[14:15], 0, v[10:11]
	v_lshl_add_u64 v[14:15], s[12:13], 0, v[10:11]
	v_lshl_add_u64 v[16:17], v[192:193], 2, s[16:17]
	v_or_b32_e32 v39, 4, v23
	v_or_b32_e32 v45, 8, v23
	v_or_b32_e32 v51, 12, v23
	v_or_b32_e32 v57, 16, v23
	v_or_b32_e32 v63, 20, v23
	v_or_b32_e32 v69, 24, v23
	v_or_b32_e32 v70, 28, v23

.LBB0_1388:
	v_add_co_u32_e32 v8, vcc, 0x55664000, v48
	s_nop 1
	v_addc_co_u32_e32 v9, vcc, 0, v49, vcc
	v_add_co_u32_e32 v6, vcc, 0x55674000, v48
	s_nop 1
	v_addc_co_u32_e32 v7, vcc, 0, v49, vcc
	ds_read_b128 v[120:123], v10 offset:0
	global_load_dword v242, v[38:39], off
	global_load_dwordx4 v[56:59], v[8:9], off offset:2048
	global_load_dwordx4 v[88:91], v[6:7], off offset:2048
	ds_read_b128 v[124:127], v10 offset:64
	global_load_dwordx4 v[60:63], v[8:9], off offset:2112
	global_load_dwordx4 v[92:95], v[6:7], off offset:2112
	ds_read_b128 v[128:131], v10 offset:128
	global_load_dwordx4 v[64:67], v[8:9], off offset:2176
	global_load_dwordx4 v[96:99], v[6:7], off offset:2176
	ds_read_b128 v[132:135], v10 offset:192
	global_load_dwordx4 v[68:71], v[8:9], off offset:2240
	global_load_dwordx4 v[100:103], v[6:7], off offset:2240
	ds_read_b128 v[136:139], v10 offset:256
	global_load_dwordx4 v[72:75], v[8:9], off offset:2304
	global_load_dwordx4 v[104:107], v[6:7], off offset:2304
	ds_read_b128 v[140:143], v10 offset:320
	global_load_dwordx4 v[76:79], v[8:9], off offset:2368
	global_load_dwordx4 v[108:111], v[6:7], off offset:2368
	ds_read_b128 v[144:147], v10 offset:384
	global_load_dwordx4 v[80:83], v[8:9], off offset:2432
	global_load_dwordx4 v[112:115], v[6:7], off offset:2432
	ds_read_b128 v[148:151], v10 offset:448
	global_load_dwordx4 v[84:87], v[8:9], off offset:2496
	global_load_dwordx4 v[116:119], v[6:7], off offset:2496
	s_waitcnt vmcnt(15) lgkmcnt(7)
	v_mfma_f32_16x16x32_bf16 v[2:5], v[120:123], v[56:59], v[2:5]
	s_waitcnt vmcnt(14)
	v_mfma_f32_16x16x32_bf16 v[2:5], v[120:123], v[88:91], v[2:5]
	ds_read_b128 v[120:123], v10 offset:512
	global_load_dwordx4 v[56:59], v[8:9], off offset:2560
	global_load_dwordx4 v[88:91], v[6:7], off offset:2560
	s_waitcnt vmcnt(15) lgkmcnt(7)
	v_mfma_f32_16x16x32_bf16 v[2:5], v[124:127], v[60:63], v[2:5]
	s_waitcnt vmcnt(14)
	v_mfma_f32_16x16x32_bf16 v[2:5], v[124:127], v[92:95], v[2:5]
	ds_read_b128 v[124:127], v10 offset:576
	global_load_dwordx4 v[60:63], v[8:9], off offset:2624
	global_load_dwordx4 v[92:95], v[6:7], off offset:2624
	s_waitcnt vmcnt(15) lgkmcnt(7)
	v_mfma_f32_16x16x32_bf16 v[2:5], v[128:131], v[64:67], v[2:5]
	s_waitcnt vmcnt(14)
	v_mfma_f32_16x16x32_bf16 v[2:5], v[128:131], v[96:99], v[2:5]
	ds_read_b128 v[128:131], v10 offset:640
	global_load_dwordx4 v[64:67], v[8:9], off offset:2688
	global_load_dwordx4 v[96:99], v[6:7], off offset:2688
	s_waitcnt vmcnt(15) lgkmcnt(7)
	v_mfma_f32_16x16x32_bf16 v[2:5], v[132:135], v[68:71], v[2:5]
	s_waitcnt vmcnt(14)
	v_mfma_f32_16x16x32_bf16 v[2:5], v[132:135], v[100:103], v[2:5]
	ds_read_b128 v[132:135], v10 offset:704
	global_load_dwordx4 v[68:71], v[8:9], off offset:2752
	global_load_dwordx4 v[100:103], v[6:7], off offset:2752
	s_waitcnt vmcnt(15) lgkmcnt(7)
	v_mfma_f32_16x16x32_bf16 v[2:5], v[136:139], v[72:75], v[2:5]
	s_waitcnt vmcnt(14)
	v_mfma_f32_16x16x32_bf16 v[2:5], v[136:139], v[104:107], v[2:5]
	ds_read_b128 v[136:139], v10 offset:768
	global_load_dwordx4 v[72:75], v[8:9], off offset:2816
	global_load_dwordx4 v[104:107], v[6:7], off offset:2816
	s_waitcnt vmcnt(15) lgkmcnt(7)
	v_mfma_f32_16x16x32_bf16 v[2:5], v[140:143], v[76:79], v[2:5]
	s_waitcnt vmcnt(14)
	v_mfma_f32_16x16x32_bf16 v[2:5], v[140:143], v[108:111], v[2:5]
	ds_read_b128 v[140:143], v10 offset:832
	global_load_dwordx4 v[76:79], v[8:9], off offset:2880
	global_load_dwordx4 v[108:111], v[6:7], off offset:2880
	s_waitcnt vmcnt(15) lgkmcnt(7)
	v_mfma_f32_16x16x32_bf16 v[2:5], v[144:147], v[80:83], v[2:5]
	s_waitcnt vmcnt(14)
	v_mfma_f32_16x16x32_bf16 v[2:5], v[144:147], v[112:115], v[2:5]
	ds_read_b128 v[144:147], v10 offset:896
	global_load_dwordx4 v[80:83], v[8:9], off offset:2944
	global_load_dwordx4 v[112:115], v[6:7], off offset:2944
	s_waitcnt vmcnt(15) lgkmcnt(7)
	v_mfma_f32_16x16x32_bf16 v[2:5], v[148:151], v[84:87], v[2:5]
	s_waitcnt vmcnt(14)
	v_mfma_f32_16x16x32_bf16 v[2:5], v[148:151], v[116:119], v[2:5]
	ds_read_b128 v[148:151], v10 offset:960
	global_load_dwordx4 v[84:87], v[8:9], off offset:3008
	global_load_dwordx4 v[116:119], v[6:7], off offset:3008
	s_waitcnt vmcnt(15) lgkmcnt(7)
	v_mfma_f32_16x16x32_bf16 v[2:5], v[120:123], v[56:59], v[2:5]
	s_waitcnt vmcnt(14)
	v_mfma_f32_16x16x32_bf16 v[2:5], v[120:123], v[88:91], v[2:5]
	ds_read_b128 v[120:123], v10 offset:1024
	global_load_dwordx4 v[56:59], v[8:9], off offset:3072
	global_load_dwordx4 v[88:91], v[6:7], off offset:3072
	s_waitcnt vmcnt(15) lgkmcnt(7)
	v_mfma_f32_16x16x32_bf16 v[2:5], v[124:127], v[60:63], v[2:5]
	s_waitcnt vmcnt(14)
	v_mfma_f32_16x16x32_bf16 v[2:5], v[124:127], v[92:95], v[2:5]
	ds_read_b128 v[124:127], v10 offset:1088
	global_load_dwordx4 v[60:63], v[8:9], off offset:3136
	global_load_dwordx4 v[92:95], v[6:7], off offset:3136
	s_waitcnt vmcnt(15) lgkmcnt(7)
	v_mfma_f32_16x16x32_bf16 v[2:5], v[128:131], v[64:67], v[2:5]
	s_waitcnt vmcnt(14)
	v_mfma_f32_16x16x32_bf16 v[2:5], v[128:131], v[96:99], v[2:5]
	ds_read_b128 v[128:131], v10 offset:1152
	global_load_dwordx4 v[64:67], v[8:9], off offset:3200
	global_load_dwordx4 v[96:99], v[6:7], off offset:3200
	s_waitcnt vmcnt(15) lgkmcnt(7)
	v_mfma_f32_16x16x32_bf16 v[2:5], v[132:135], v[68:71], v[2:5]
	s_waitcnt vmcnt(14)
	v_mfma_f32_16x16x32_bf16 v[2:5], v[132:135], v[100:103], v[2:5]
	ds_read_b128 v[132:135], v10 offset:1216
	global_load_dwordx4 v[68:71], v[8:9], off offset:3264
	global_load_dwordx4 v[100:103], v[6:7], off offset:3264
	s_waitcnt vmcnt(15) lgkmcnt(7)
	v_mfma_f32_16x16x32_bf16 v[2:5], v[136:139], v[72:75], v[2:5]
	s_waitcnt vmcnt(14)
	v_mfma_f32_16x16x32_bf16 v[2:5], v[136:139], v[104:107], v[2:5]
	ds_read_b128 v[136:139], v10 offset:1280
	global_load_dwordx4 v[72:75], v[8:9], off offset:3328
	global_load_dwordx4 v[104:107], v[6:7], off offset:3328
	s_waitcnt vmcnt(15) lgkmcnt(7)
	v_mfma_f32_16x16x32_bf16 v[2:5], v[140:143], v[76:79], v[2:5]
	s_waitcnt vmcnt(14)
	v_mfma_f32_16x16x32_bf16 v[2:5], v[140:143], v[108:111], v[2:5]
	ds_read_b128 v[140:143], v10 offset:1344
	global_load_dwordx4 v[76:79], v[8:9], off offset:3392
	global_load_dwordx4 v[108:111], v[6:7], off offset:3392
	s_waitcnt vmcnt(15) lgkmcnt(7)
	v_mfma_f32_16x16x32_bf16 v[2:5], v[144:147], v[80:83], v[2:5]
	s_waitcnt vmcnt(14)
	v_mfma_f32_16x16x32_bf16 v[2:5], v[144:147], v[112:115], v[2:5]
	ds_read_b128 v[144:147], v10 offset:1408
	global_load_dwordx4 v[80:83], v[8:9], off offset:3456
	global_load_dwordx4 v[112:115], v[6:7], off offset:3456
	s_waitcnt vmcnt(15) lgkmcnt(7)
	v_mfma_f32_16x16x32_bf16 v[2:5], v[148:151], v[84:87], v[2:5]
	s_waitcnt vmcnt(14)
	v_mfma_f32_16x16x32_bf16 v[2:5], v[148:151], v[116:119], v[2:5]
	ds_read_b128 v[148:151], v10 offset:1472
	global_load_dwordx4 v[84:87], v[8:9], off offset:3520
	global_load_dwordx4 v[116:119], v[6:7], off offset:3520
	s_waitcnt vmcnt(15) lgkmcnt(7)
	v_mfma_f32_16x16x32_bf16 v[2:5], v[120:123], v[56:59], v[2:5]
	s_waitcnt vmcnt(14)
	v_mfma_f32_16x16x32_bf16 v[2:5], v[120:123], v[88:91], v[2:5]
	ds_read_b128 v[120:123], v10 offset:1536
	global_load_dwordx4 v[56:59], v[8:9], off offset:3584
	global_load_dwordx4 v[88:91], v[6:7], off offset:3584
	s_waitcnt vmcnt(15) lgkmcnt(7)
	v_mfma_f32_16x16x32_bf16 v[2:5], v[124:127], v[60:63], v[2:5]
	s_waitcnt vmcnt(14)
	v_mfma_f32_16x16x32_bf16 v[2:5], v[124:127], v[92:95], v[2:5]
	ds_read_b128 v[124:127], v10 offset:1600
	global_load_dwordx4 v[60:63], v[8:9], off offset:3648
	global_load_dwordx4 v[92:95], v[6:7], off offset:3648
	s_waitcnt vmcnt(15) lgkmcnt(7)
	v_mfma_f32_16x16x32_bf16 v[2:5], v[128:131], v[64:67], v[2:5]
	s_waitcnt vmcnt(14)
	v_mfma_f32_16x16x32_bf16 v[2:5], v[128:131], v[96:99], v[2:5]
	ds_read_b128 v[128:131], v10 offset:1664
	global_load_dwordx4 v[64:67], v[8:9], off offset:3712
	global_load_dwordx4 v[96:99], v[6:7], off offset:3712
	s_waitcnt vmcnt(15) lgkmcnt(7)
	v_mfma_f32_16x16x32_bf16 v[2:5], v[132:135], v[68:71], v[2:5]
	s_waitcnt vmcnt(14)
	v_mfma_f32_16x16x32_bf16 v[2:5], v[132:135], v[100:103], v[2:5]
	ds_read_b128 v[132:135], v10 offset:1728
	global_load_dwordx4 v[68:71], v[8:9], off offset:3776
	global_load_dwordx4 v[100:103], v[6:7], off offset:3776
	s_waitcnt vmcnt(15) lgkmcnt(7)
	v_mfma_f32_16x16x32_bf16 v[2:5], v[136:139], v[72:75], v[2:5]
	s_waitcnt vmcnt(14)
	v_mfma_f32_16x16x32_bf16 v[2:5], v[136:139], v[104:107], v[2:5]
	ds_read_b128 v[136:139], v10 offset:1792
	global_load_dwordx4 v[72:75], v[8:9], off offset:3840
	global_load_dwordx4 v[104:107], v[6:7], off offset:3840
	s_waitcnt vmcnt(15) lgkmcnt(7)
	v_mfma_f32_16x16x32_bf16 v[2:5], v[140:143], v[76:79], v[2:5]
	s_waitcnt vmcnt(14)
	v_mfma_f32_16x16x32_bf16 v[2:5], v[140:143], v[108:111], v[2:5]
	ds_read_b128 v[140:143], v10 offset:1856
	global_load_dwordx4 v[76:79], v[8:9], off offset:3904
	global_load_dwordx4 v[108:111], v[6:7], off offset:3904
	s_waitcnt vmcnt(15) lgkmcnt(7)
	v_mfma_f32_16x16x32_bf16 v[2:5], v[144:147], v[80:83], v[2:5]
	s_waitcnt vmcnt(14)
	v_mfma_f32_16x16x32_bf16 v[2:5], v[144:147], v[112:115], v[2:5]
	ds_read_b128 v[144:147], v10 offset:1920
	global_load_dwordx4 v[80:83], v[8:9], off offset:3968
	global_load_dwordx4 v[112:115], v[6:7], off offset:3968
	s_waitcnt vmcnt(15) lgkmcnt(7)
	v_mfma_f32_16x16x32_bf16 v[2:5], v[148:151], v[84:87], v[2:5]
	s_waitcnt vmcnt(14)
	v_mfma_f32_16x16x32_bf16 v[2:5], v[148:151], v[116:119], v[2:5]
	ds_read_b128 v[148:151], v10 offset:1984
	global_load_dwordx4 v[84:87], v[8:9], off offset:4032
	global_load_dwordx4 v[116:119], v[6:7], off offset:4032
	s_waitcnt vmcnt(15) lgkmcnt(7)
	v_mfma_f32_16x16x32_bf16 v[2:5], v[120:123], v[56:59], v[2:5]
	s_waitcnt vmcnt(14)
	v_mfma_f32_16x16x32_bf16 v[2:5], v[120:123], v[88:91], v[2:5]
	s_waitcnt vmcnt(13) lgkmcnt(6)
	v_mfma_f32_16x16x32_bf16 v[2:5], v[124:127], v[60:63], v[2:5]
	s_waitcnt vmcnt(12)
	v_mfma_f32_16x16x32_bf16 v[2:5], v[124:127], v[92:95], v[2:5]
	s_waitcnt vmcnt(11) lgkmcnt(5)
	v_mfma_f32_16x16x32_bf16 v[2:5], v[128:131], v[64:67], v[2:5]
	s_waitcnt vmcnt(10)
	v_mfma_f32_16x16x32_bf16 v[2:5], v[128:131], v[96:99], v[2:5]
	s_waitcnt vmcnt(9) lgkmcnt(4)
	v_mfma_f32_16x16x32_bf16 v[2:5], v[132:135], v[68:71], v[2:5]
	s_waitcnt vmcnt(8)
	v_mfma_f32_16x16x32_bf16 v[2:5], v[132:135], v[100:103], v[2:5]
	s_waitcnt vmcnt(7) lgkmcnt(3)
	v_mfma_f32_16x16x32_bf16 v[2:5], v[136:139], v[72:75], v[2:5]
	s_waitcnt vmcnt(6)
	v_mfma_f32_16x16x32_bf16 v[2:5], v[136:139], v[104:107], v[2:5]
	s_waitcnt vmcnt(5) lgkmcnt(2)
	v_mfma_f32_16x16x32_bf16 v[2:5], v[140:143], v[76:79], v[2:5]
	s_waitcnt vmcnt(4)
	v_mfma_f32_16x16x32_bf16 v[2:5], v[140:143], v[108:111], v[2:5]
	s_waitcnt vmcnt(3) lgkmcnt(1)
	v_mfma_f32_16x16x32_bf16 v[2:5], v[144:147], v[80:83], v[2:5]
	s_waitcnt vmcnt(2)
	v_mfma_f32_16x16x32_bf16 v[2:5], v[144:147], v[112:115], v[2:5]
	s_waitcnt vmcnt(1) lgkmcnt(0)
	v_mfma_f32_16x16x32_bf16 v[2:5], v[148:151], v[84:87], v[2:5]
	s_waitcnt vmcnt(0)
	v_mfma_f32_16x16x32_bf16 v[2:5], v[148:151], v[116:119], v[2:5]
	s_nop 0
	s_nop 6
	s_nop 0
	v_add_f32_e32 v2, v2, v242
	v_add_f32_e32 v3, v3, v242
	v_add_f32_e32 v4, v4, v242
	v_add_f32_e32 v5, v5, v242
	ds_write2_b32 v196, v2, v3 offset1:33
	ds_write2_b32 v196, v4, v5 offset0:66 offset1:99
	s_waitcnt lgkmcnt(0)
	s_barrier
	s_and_saveexec_b64 s[0:1], s[14:15]
	s_cbranch_execz .LBB0_1765
	ds_read2_b32 v[6:7], v192 offset1:1
	s_mov_b32 s2, 0xff800000
	v_mov_b32_e32 v3, 0xff800000
	v_mov_b32_e32 v8, 0xff800000
	v_mov_b32_e32 v2, 0
	s_waitcnt lgkmcnt(0)
	v_cmp_lg_f32_e32 vcc, s2, v6
	v_mov_b32_e32 v4, 0
	v_mov_b32_e32 v5, 0
	v_cndmask_b32_e32 v6, v3, v6, vcc
	v_cmp_lt_f32_e32 vcc, s2, v7
	v_mov_b32_e32 v3, 0
	v_mov_b32_e32 v10, 0xff800000
	v_mov_b32_e32 v9, 0xff800000
	s_and_saveexec_b64 s[2:3], vcc
	s_cbranch_execz .LBB0_1404
	v_cmp_ngt_f32_e32 vcc, v7, v6
	s_and_saveexec_b64 s[4:5], vcc
	s_xor_b64 s[10:11], exec, s[4:5]
	s_cbranch_execz .LBB0_1401
	v_cmp_ngt_f32_e32 vcc, v7, v8
	s_and_saveexec_b64 s[4:5], vcc
	s_xor_b64 s[18:19], exec, s[4:5]
	s_cbranch_execz .LBB0_1398
	v_cmp_ngt_f32_e32 vcc, v7, v8
	s_and_saveexec_b64 s[4:5], vcc
	s_xor_b64 s[20:21], exec, s[4:5]
	v_mov_b32_e32 v8, 0xff800000
	v_mov_b32_e32 v10, 0xff800000
	s_or_saveexec_b64 s[20:21], s[20:21]
	v_mov_b32_e32 v4, 0
	v_mov_b32_e32 v5, 1
	v_mov_b32_e32 v9, v7
	s_xor_b64 exec, exec, s[20:21]
	v_mov_b32_e32 v8, 0xff800000
	v_mov_b32_e32 v9, 0xff800000
	v_mov_b32_e32 v5, 0
	v_mov_b32_e32 v10, v7
	v_mov_b32_e32 v4, 1
	s_or_b64 exec, exec, s[20:21]
